# grid barrier variant: the last arriver increments every XCD's generation word itself; all other workgroups (XCD-last ones included) wait on their own XCD's word (32 pollers per word, no second release
# speedup vs baseline: 1.0013x; 1.0013x over previous
.LBB0_83:
	s_or_b64 exec, exec, s[10:11]
	v_cvt_f32_u32_e32 v3, v0
	s_waitcnt vmcnt(0)
	v_readfirstlane_b32 s0, v2
	s_add_u32 s10, s26, 0x7500
	s_addc_u32 s11, s27, 0
	v_rcp_iflag_f32_e32 v3, v3
	v_add_u32_e32 v1, s0, v1
	v_add_u32_e32 v4, 1, v1
	s_mov_b64 s[12:13], -1
	v_mul_f32_e32 v2, 0x4f7ffffe, v3
	v_cvt_u32_f32_e32 v2, v2
	v_sub_u32_e32 v3, 0, v0
	v_mul_lo_u32 v3, v3, v2
	v_mul_hi_u32 v3, v2, v3
	v_add_u32_e32 v2, v2, v3
	v_mul_hi_u32 v2, v1, v2
	v_mul_lo_u32 v3, v2, v0
	v_sub_u32_e32 v1, v1, v3
	v_add_u32_e32 v5, 1, v2
	v_cmp_ge_u32_e32 vcc, v1, v0
	v_sub_u32_e32 v3, v1, v0
	s_nop 0
	v_cndmask_b32_e32 v2, v2, v5, vcc
	v_cndmask_b32_e32 v1, v1, v3, vcc
	v_add_u32_e32 v3, 1, v2
	v_cmp_ge_u32_e32 vcc, v1, v0
	s_nop 1
	v_cndmask_b32_e32 v2, v2, v3, vcc
	v_mul_lo_u32 v1, v0, v2
	v_add_u32_e32 v0, v1, v0
	v_cmp_ne_u32_e32 vcc, v4, v0
	v_mov_b64_e32 v[0:1], s[10:11]
	s_and_saveexec_b64 s[8:9], vcc
	s_cbranch_execz .LBB0_95
	v_mov_b32_e32 v0, 0
	v_mov_b32_e32 v3, 0x2000
	global_load_dword v1, v3, s[6:7] offset:1024 sc1
	s_mov_b64 s[16:17], 0
	s_waitcnt vmcnt(0)
	v_cmp_eq_u32_e32 vcc, v1, v2
	s_and_saveexec_b64 s[14:15], vcc
	s_cbranch_execz .LBB0_94
	s_add_u32 s12, s26, 0x4200
	s_addc_u32 s13, s27, 0
	s_mov_b32 s0, 1
	s_branch .LBB0_87

.LBB0_89:
	global_load_dword v1, v3, s[6:7] offset:1024 sc1
	s_add_i32 s0, s0, 1
	s_mov_b64 s[20:21], -1
	s_waitcnt vmcnt(0)
	v_cmp_ne_u32_e32 vcc, v1, v2
	s_orn2_b64 s[28:29], vcc, exec
	s_branch .LBB0_86

.LBB0_95:
	s_or_b64 exec, exec, s[8:9]
	s_and_saveexec_b64 s[8:9], s[12:13]
	s_cbranch_execz .LBB0_97
	v_mov_b32_e32 v2, 1
	v_mov_b32_e32 v3, 0x6400
	global_atomic_add v3, v2, s[26:27]
	global_atomic_add v3, v2, s[26:27] offset:256
	global_atomic_add v3, v2, s[26:27] offset:512
	global_atomic_add v3, v2, s[26:27] offset:768
	global_atomic_add v3, v2, s[26:27] offset:1024
	global_atomic_add v3, v2, s[26:27] offset:1280
	global_atomic_add v3, v2, s[26:27] offset:1536
	global_atomic_add v3, v2, s[26:27] offset:1792
	global_atomic_add v3, v2, s[26:27] offset:2048
	global_atomic_add v3, v2, s[26:27] offset:2304
	global_atomic_add v3, v2, s[26:27] offset:2560
	global_atomic_add v3, v2, s[26:27] offset:2816
	global_atomic_add v3, v2, s[26:27] offset:3072
	global_atomic_add v3, v2, s[26:27] offset:3328
	global_atomic_add v3, v2, s[26:27] offset:3584
	global_atomic_add v3, v2, s[26:27] offset:3840
